# expert GEMM K-loops: B half-1 stage of the second K-tile moved from phase 4 to phase 1 of the next trip (pieces 4/4/4/4)
# baseline (speedup 1.0000x reference)
.LBB0_910:
	s_add_u32 s25, s36, 0x100
	s_addc_u32 s27, s37, 0
	s_lshl_b32 s7, s55, 10
	s_add_i32 s7, s7, 0x24000
	s_mov_b32 s42, -2
	s_mov_b64 s[36:37], 0
	s_cmp_eq_u32 s42, 12
	s_cselect_b64 s[40:41], -1, 0
	s_and_b64 s[38:39], s[34:35], s[40:41]
	s_andn2_b64 vcc, exec, s[38:39]
	v_mov_b32_e32 v128, v186
	v_mov_b32_e32 v129, v176
	s_add_u32 s76, s10, s36
	v_add_u32_e32 v134, s67, v194
	v_add_u32_e32 v142, s67, v195
	v_add_u32_e32 v150, s68, v194
	v_add_u32_e32 v158, s68, v195
	s_addc_u32 s77, s11, s37
	ds_read_b128 v[130:133], v134
	ds_read_b128 v[138:141], v134 offset:2048
	ds_read_b128 v[134:137], v142
	ds_read_b128 v[142:145], v142 offset:2048
	ds_read_b128 v[146:149], v150
	ds_read_b128 v[154:157], v150 offset:2048
	ds_read_b128 v[150:153], v158
	ds_read_b128 v[158:161], v158 offset:2048
	s_add_u32 s43, s76, 0x36000100
	s_addc_u32 s75, s77, 0
	s_and_b64 s[38:39], s[40:41], exec
	s_cselect_b32 s39, s13, s75
	s_cselect_b32 s38, s12, s43
	s_add_u32 s43, s25, s36
	s_addc_u32 s75, s27, s37
	s_and_b64 s[40:41], s[40:41], exec
	s_cselect_b32 s41, s31, s75
	s_cselect_b32 s40, s30, s43
	ds_read_b128 v[162:165], v227
	ds_read_b128 v[232:235], v227 offset:2048
	ds_read_b128 v[166:169], v228
	ds_read_b128 v[236:239], v228 offset:2048
	ds_read_b128 v[240:243], v227 offset:4096
	ds_read_b128 v[196:199], v227 offset:6144
	ds_read_b128 v[244:247], v228 offset:4096
	ds_read_b128 v[200:203], v228 offset:6144
	s_add_u32 vcc_lo, s43, 0x3f80
	s_addc_u32 vcc_hi, s75, 0
	s_add_i32 m0, s5, 0x1c000
	s_nop 0
	global_load_lds_dwordx4 v184, vcc
	s_add_i32 m0, s5, 0x1e000
	s_nop 0
	global_load_lds_dwordx4 v178, vcc
	s_add_i32 m0, s50, 0xc000
	s_add_u32 vcc_lo, s76, s16
	s_addc_u32 vcc_hi, s77, s17
	v_mov_b32_e32 v187, v177
	global_load_lds_dwordx4 v176, vcc
	s_add_i32 m0, s50, 0xe000
	s_nop 0
	global_load_lds_dwordx4 v186, vcc
	s_waitcnt vmcnt(8)
	s_waitcnt lgkmcnt(0)
	s_barrier
	s_setprio 1
	s_waitcnt lgkmcnt(0)
	v_mfma_f32_16x16x128_f8f6f4 v[100:103], v[130:137], v[162:169], 0
	v_mfma_f32_16x16x128_f8f6f4 v[96:99], v[138:145], v[162:169], 0
	v_mfma_f32_16x16x128_f8f6f4 v[92:95], v[130:137], v[232:239], 0
	v_mfma_f32_16x16x128_f8f6f4 v[88:91], v[138:145], v[232:239], 0
	v_mfma_f32_16x16x128_f8f6f4 v[84:87], v[130:137], v[240:247], 0
	v_mfma_f32_16x16x128_f8f6f4 v[80:83], v[138:145], v[240:247], 0
	v_mfma_f32_16x16x128_f8f6f4 v[170:173], v[130:137], v[196:203], 0
	v_mfma_f32_16x16x128_f8f6f4 v[188:191], v[138:145], v[196:203], 0
	s_setprio 0
	s_setprio 1
	v_mfma_f32_16x16x128_f8f6f4 v[40:43], v[146:153], v[196:203], 0
	v_mfma_f32_16x16x128_f8f6f4 v[32:35], v[154:161], v[196:203], 0
	v_mfma_f32_16x16x128_f8f6f4 v[248:251], v[146:153], v[162:169], 0
	v_mfma_f32_16x16x128_f8f6f4 v[204:207], v[154:161], v[162:169], 0
	v_mfma_f32_16x16x128_f8f6f4 v[208:211], v[146:153], v[232:239], 0
	v_mfma_f32_16x16x128_f8f6f4 v[212:215], v[154:161], v[232:239], 0
	v_mfma_f32_16x16x128_f8f6f4 v[216:219], v[146:153], v[240:247], 0
	v_mfma_f32_16x16x128_f8f6f4 v[240:243], v[154:161], v[240:247], 0
	s_setprio 0
	s_barrier
	s_add_i32 s43, s67, s5
	s_mov_b32 m0, s43
	s_nop 2
	ds_read_b128 v[48:51], v227 offset:16384
	ds_read_b128 v[56:59], v227 offset:18432
	ds_read_b128 v[52:55], v228 offset:16384
	ds_read_b128 v[60:63], v228 offset:18432
	ds_read_b128 v[64:67], v227 offset:20480
	ds_read_b128 v[72:75], v227 offset:22528
	ds_read_b128 v[68:71], v228 offset:20480
	ds_read_b128 v[76:79], v228 offset:22528
	s_nop 0
	global_load_lds_dwordx4 v184, s[40:41]
	s_add_i32 m0, s43, 0x2000
	s_add_u32 s76, s40, 0x4000
	s_addc_u32 s77, s41, 0
	s_add_i32 s43, s68, s5
	s_nop 0
	global_load_lds_dwordx4 v178, s[40:41]
	s_mov_b32 m0, s43
	s_nop 0
	global_load_lds_dwordx4 v184, s[76:77]
	s_add_i32 m0, s43, 0x2000
	s_nop 0
	global_load_lds_dwordx4 v178, s[76:77]
	s_waitcnt vmcnt(6)
	s_waitcnt lgkmcnt(0)
	s_barrier
	s_setprio 1
	s_waitcnt lgkmcnt(0)
	v_mfma_f32_16x16x128_f8f6f4 v[44:47], v[130:137], v[48:55], 0
	v_mfma_f32_16x16x128_f8f6f4 v[36:39], v[138:145], v[48:55], 0
	v_mfma_f32_16x16x128_f8f6f4 v[28:31], v[130:137], v[56:63], 0
	v_mfma_f32_16x16x128_f8f6f4 v[24:27], v[138:145], v[56:63], 0
	v_mfma_f32_16x16x128_f8f6f4 v[20:23], v[130:137], v[64:71], 0
	v_mfma_f32_16x16x128_f8f6f4 v[16:19], v[138:145], v[64:71], 0
	v_mfma_f32_16x16x128_f8f6f4 v[12:15], v[130:137], v[72:79], 0
	v_mfma_f32_16x16x128_f8f6f4 v[8:11], v[138:145], v[72:79], 0
	s_setprio 0
	s_setprio 1
	v_mfma_f32_16x16x128_f8f6f4 v[4:7], v[146:153], v[48:55], 0
	v_mfma_f32_16x16x128_f8f6f4 v[0:3], v[154:161], v[48:55], 0
	v_mfma_f32_16x16x128_f8f6f4 v[104:107], v[146:153], v[56:63], 0
	v_mfma_f32_16x16x128_f8f6f4 v[108:111], v[154:161], v[56:63], 0
	v_mfma_f32_16x16x128_f8f6f4 v[112:115], v[146:153], v[64:71], 0
	v_mfma_f32_16x16x128_f8f6f4 v[116:119], v[154:161], v[64:71], 0
	v_mfma_f32_16x16x128_f8f6f4 v[120:123], v[146:153], v[72:79], 0
	v_mfma_f32_16x16x128_f8f6f4 v[124:127], v[154:161], v[72:79], 0
	s_setprio 0
	s_barrier
	s_add_i32 s43, 0, 0x18000
	v_add_u32_e32 v48, s43, v194
	s_add_i32 s75, 0, 0x1c000
	v_add_u32_e32 v49, s43, v195
	ds_read_b128 v[130:133], v48
	ds_read_b128 v[138:141], v48 offset:2048
	ds_read_b128 v[134:137], v49
	ds_read_b128 v[142:145], v49 offset:2048
	v_add_u32_e32 v48, s75, v194
	v_add_u32_e32 v49, s75, v195
	ds_read_b128 v[146:149], v48
	ds_read_b128 v[154:157], v48 offset:2048
	ds_read_b128 v[150:153], v49
	ds_read_b128 v[158:161], v49 offset:2048
	s_mov_b32 m0, s52
	v_mov_b32_e32 v176, v129
	ds_read_b128 v[48:51], v227 offset:32768
	ds_read_b128 v[162:165], v227 offset:34816
	ds_read_b128 v[52:55], v228 offset:32768
	ds_read_b128 v[166:169], v228 offset:34816
	ds_read_b128 v[196:199], v227 offset:36864
	ds_read_b128 v[232:235], v227 offset:38912
	ds_read_b128 v[200:203], v228 offset:36864
	ds_read_b128 v[236:239], v228 offset:38912
	s_mov_b32 m0, s50
	s_nop 0
	global_load_lds_dwordx4 v180, s[38:39]
	s_mov_b32 m0, s51
	s_nop 0
	global_load_lds_dwordx4 v182, s[38:39]
	s_mov_b32 m0, s52
	v_mov_b32_e32 v186, v128
	global_load_lds_dwordx4 v176, s[38:39]
	s_mov_b32 m0, s53
	s_nop 0
	global_load_lds_dwordx4 v186, s[38:39]
	s_waitcnt vmcnt(8)
	s_waitcnt lgkmcnt(0)
	s_barrier
	s_setprio 1
	s_waitcnt lgkmcnt(0)
	v_mfma_f32_16x16x128_f8f6f4 v[100:103], v[130:137], v[48:55], v[100:103]
	v_mfma_f32_16x16x128_f8f6f4 v[96:99], v[138:145], v[48:55], v[96:99]
	v_mfma_f32_16x16x128_f8f6f4 v[92:95], v[130:137], v[162:169], v[92:95]
	v_mfma_f32_16x16x128_f8f6f4 v[88:91], v[138:145], v[162:169], v[88:91]
	v_mfma_f32_16x16x128_f8f6f4 v[84:87], v[130:137], v[196:203], v[84:87]
	v_mfma_f32_16x16x128_f8f6f4 v[80:83], v[138:145], v[196:203], v[80:83]
	v_mfma_f32_16x16x128_f8f6f4 v[76:79], v[130:137], v[232:239], v[170:173]
	v_mfma_f32_16x16x128_f8f6f4 v[72:75], v[138:145], v[232:239], v[188:191]
	s_setprio 0
	s_setprio 1
	v_mfma_f32_16x16x128_f8f6f4 v[68:71], v[146:153], v[48:55], v[248:251]
	v_mfma_f32_16x16x128_f8f6f4 v[64:67], v[154:161], v[48:55], v[204:207]
	v_mfma_f32_16x16x128_f8f6f4 v[60:63], v[146:153], v[162:169], v[208:211]
	v_mfma_f32_16x16x128_f8f6f4 v[56:59], v[154:161], v[162:169], v[212:215]
	v_mfma_f32_16x16x128_f8f6f4 v[52:55], v[146:153], v[196:203], v[216:219]
	v_mfma_f32_16x16x128_f8f6f4 v[48:51], v[154:161], v[196:203], v[240:243]
	v_mfma_f32_16x16x128_f8f6f4 v[40:43], v[146:153], v[232:239], v[40:43]
	v_mfma_f32_16x16x128_f8f6f4 v[32:35], v[154:161], v[232:239], v[32:35]
	s_setprio 0
	s_barrier
	v_mov_b32_e32 v185, v177
	ds_read_b128 v[162:165], v227 offset:49152
	ds_read_b128 v[196:199], v227 offset:51200
	ds_read_b128 v[166:169], v228 offset:49152
	ds_read_b128 v[200:203], v228 offset:51200
	ds_read_b128 v[232:235], v227 offset:53248
	ds_read_b128 v[240:243], v227 offset:55296
	ds_read_b128 v[236:239], v228 offset:53248
	ds_read_b128 v[244:247], v228 offset:55296
	s_add_i32 s43, s43, s5
	s_add_u32 vcc_lo, s40, s14
	s_addc_u32 vcc_hi, s41, s15
	s_mov_b32 m0, s43
	v_mov_b32_e32 v179, v177
	global_load_lds_dwordx4 v184, vcc
	s_add_i32 m0, s43, 0x2000
	v_mov_b32_e32 v181, v177
	global_load_lds_dwordx4 v178, vcc
	v_mov_b32_e32 v183, v177
	s_mov_b32 m0, s62
	s_add_u32 vcc_lo, s38, s14
	s_addc_u32 vcc_hi, s39, s15
	global_load_lds_dwordx4 v180, vcc
	s_mov_b32 m0, s63
	s_nop 0
	global_load_lds_dwordx4 v182, vcc
	s_waitcnt vmcnt(6)
	s_waitcnt lgkmcnt(0)
	s_barrier
	s_setprio 1
	s_waitcnt lgkmcnt(0)
	v_mfma_f32_16x16x128_f8f6f4 v[44:47], v[130:137], v[162:169], v[44:47]
	v_mfma_f32_16x16x128_f8f6f4 v[36:39], v[138:145], v[162:169], v[36:39]
	v_mfma_f32_16x16x128_f8f6f4 v[28:31], v[130:137], v[196:203], v[28:31]
	v_mfma_f32_16x16x128_f8f6f4 v[24:27], v[138:145], v[196:203], v[24:27]
	v_mfma_f32_16x16x128_f8f6f4 v[20:23], v[130:137], v[232:239], v[20:23]
	v_mfma_f32_16x16x128_f8f6f4 v[16:19], v[138:145], v[232:239], v[16:19]
	v_mfma_f32_16x16x128_f8f6f4 v[12:15], v[130:137], v[240:247], v[12:15]
	v_mfma_f32_16x16x128_f8f6f4 v[8:11], v[138:145], v[240:247], v[8:11]
	s_setprio 0
	s_setprio 1
	v_mfma_f32_16x16x128_f8f6f4 v[4:7], v[146:153], v[162:169], v[4:7]
	v_mfma_f32_16x16x128_f8f6f4 v[0:3], v[154:161], v[162:169], v[0:3]
	v_mfma_f32_16x16x128_f8f6f4 v[104:107], v[146:153], v[196:203], v[104:107]
	v_mfma_f32_16x16x128_f8f6f4 v[108:111], v[154:161], v[196:203], v[108:111]
	v_mfma_f32_16x16x128_f8f6f4 v[112:115], v[146:153], v[232:239], v[112:115]
	v_mfma_f32_16x16x128_f8f6f4 v[116:119], v[154:161], v[232:239], v[116:119]
	v_mfma_f32_16x16x128_f8f6f4 v[120:123], v[146:153], v[240:247], v[120:123]
	v_mfma_f32_16x16x128_f8f6f4 v[124:127], v[154:161], v[240:247], v[124:127]
	s_setprio 0
	s_barrier
	s_add_i32 s42, s42, 2
	s_add_u32 s36, s36, 0x100
	s_addc_u32 s37, s37, 0
	s_branch .LBB0_912
.LBB0_911:
	s_add_u32 s76, s10, s36
	v_add_u32_e32 v134, s67, v194
	v_add_u32_e32 v142, s67, v195
	v_add_u32_e32 v150, s68, v194
	v_add_u32_e32 v158, s68, v195
	s_addc_u32 s77, s11, s37
	ds_read_b128 v[130:133], v134
	ds_read_b128 v[138:141], v134 offset:2048
	ds_read_b128 v[134:137], v142
	ds_read_b128 v[142:145], v142 offset:2048
	ds_read_b128 v[146:149], v150
	ds_read_b128 v[154:157], v150 offset:2048
	ds_read_b128 v[150:153], v158
	ds_read_b128 v[158:161], v158 offset:2048
	s_add_u32 s43, s76, 0x36000100
	s_addc_u32 s75, s77, 0
	s_and_b64 s[38:39], s[40:41], exec
	s_cselect_b32 s39, s13, s75
	s_cselect_b32 s38, s12, s43
	s_add_u32 s43, s25, s36
	s_addc_u32 s75, s27, s37
	s_and_b64 s[40:41], s[40:41], exec
	s_cselect_b32 s41, s31, s75
	s_cselect_b32 s40, s30, s43
	ds_read_b128 v[162:165], v227
	ds_read_b128 v[232:235], v227 offset:2048
	ds_read_b128 v[166:169], v228
	ds_read_b128 v[236:239], v228 offset:2048
	ds_read_b128 v[240:243], v227 offset:4096
	ds_read_b128 v[196:199], v227 offset:6144
	ds_read_b128 v[244:247], v228 offset:4096
	ds_read_b128 v[200:203], v228 offset:6144
	s_add_u32 vcc_lo, s43, 0x3f80
	s_addc_u32 vcc_hi, s75, 0
	s_add_i32 m0, s5, 0x1c000
	s_nop 0
	global_load_lds_dwordx4 v184, vcc
	s_add_i32 m0, s5, 0x1e000
	s_nop 0
	global_load_lds_dwordx4 v178, vcc
	s_add_i32 m0, s50, 0xc000
	s_add_u32 vcc_lo, s76, s16
	s_addc_u32 vcc_hi, s77, s17
	v_mov_b32_e32 v187, v177
	global_load_lds_dwordx4 v176, vcc
	s_add_i32 m0, s50, 0xe000
	s_nop 0
	global_load_lds_dwordx4 v186, vcc
	s_waitcnt vmcnt(8)
	s_waitcnt lgkmcnt(0)
	s_barrier
	s_setprio 1
	s_waitcnt lgkmcnt(0)
	v_mfma_f32_16x16x128_f8f6f4 v[100:103], v[130:137], v[162:169], v[100:103]
	v_mfma_f32_16x16x128_f8f6f4 v[96:99], v[138:145], v[162:169], v[96:99]
	v_mfma_f32_16x16x128_f8f6f4 v[92:95], v[130:137], v[232:239], v[92:95]
	v_mfma_f32_16x16x128_f8f6f4 v[88:91], v[138:145], v[232:239], v[88:91]
	v_mfma_f32_16x16x128_f8f6f4 v[84:87], v[130:137], v[240:247], v[84:87]
	v_mfma_f32_16x16x128_f8f6f4 v[80:83], v[138:145], v[240:247], v[80:83]
	v_mfma_f32_16x16x128_f8f6f4 v[170:173], v[130:137], v[196:203], v[76:79]
	v_mfma_f32_16x16x128_f8f6f4 v[188:191], v[138:145], v[196:203], v[72:75]
	s_setprio 0
	s_setprio 1
	v_mfma_f32_16x16x128_f8f6f4 v[40:43], v[146:153], v[196:203], v[40:43]
	v_mfma_f32_16x16x128_f8f6f4 v[32:35], v[154:161], v[196:203], v[32:35]
	v_mfma_f32_16x16x128_f8f6f4 v[248:251], v[146:153], v[162:169], v[68:71]
	v_mfma_f32_16x16x128_f8f6f4 v[204:207], v[154:161], v[162:169], v[64:67]
	v_mfma_f32_16x16x128_f8f6f4 v[208:211], v[146:153], v[232:239], v[60:63]
	v_mfma_f32_16x16x128_f8f6f4 v[212:215], v[154:161], v[232:239], v[56:59]
	v_mfma_f32_16x16x128_f8f6f4 v[216:219], v[146:153], v[240:247], v[52:55]
	v_mfma_f32_16x16x128_f8f6f4 v[240:243], v[154:161], v[240:247], v[48:51]
	s_setprio 0
	s_barrier
	s_add_i32 s43, s67, s5
	s_mov_b32 m0, s43
	s_nop 2
	ds_read_b128 v[48:51], v227 offset:16384
	ds_read_b128 v[56:59], v227 offset:18432
	ds_read_b128 v[52:55], v228 offset:16384
	ds_read_b128 v[60:63], v228 offset:18432
	ds_read_b128 v[64:67], v227 offset:20480
	ds_read_b128 v[72:75], v227 offset:22528
	ds_read_b128 v[68:71], v228 offset:20480
	ds_read_b128 v[76:79], v228 offset:22528
	s_nop 0
	global_load_lds_dwordx4 v184, s[40:41]
	s_add_i32 m0, s43, 0x2000
	s_add_u32 s76, s40, 0x4000
	s_addc_u32 s77, s41, 0
	s_add_i32 s43, s68, s5
	s_nop 0
	global_load_lds_dwordx4 v178, s[40:41]
	s_mov_b32 m0, s43
	s_nop 0
	global_load_lds_dwordx4 v184, s[76:77]
	s_add_i32 m0, s43, 0x2000
	s_nop 0
	global_load_lds_dwordx4 v178, s[76:77]
	s_waitcnt vmcnt(6)
	s_waitcnt lgkmcnt(0)
	s_barrier
	s_setprio 1
	s_waitcnt lgkmcnt(0)
	v_mfma_f32_16x16x128_f8f6f4 v[44:47], v[130:137], v[48:55], v[44:47]
	v_mfma_f32_16x16x128_f8f6f4 v[36:39], v[138:145], v[48:55], v[36:39]
	v_mfma_f32_16x16x128_f8f6f4 v[28:31], v[130:137], v[56:63], v[28:31]
	v_mfma_f32_16x16x128_f8f6f4 v[24:27], v[138:145], v[56:63], v[24:27]
	v_mfma_f32_16x16x128_f8f6f4 v[20:23], v[130:137], v[64:71], v[20:23]
	v_mfma_f32_16x16x128_f8f6f4 v[16:19], v[138:145], v[64:71], v[16:19]
	v_mfma_f32_16x16x128_f8f6f4 v[12:15], v[130:137], v[72:79], v[12:15]
	v_mfma_f32_16x16x128_f8f6f4 v[8:11], v[138:145], v[72:79], v[8:11]
	s_setprio 0
	s_setprio 1
	v_mfma_f32_16x16x128_f8f6f4 v[4:7], v[146:153], v[48:55], v[4:7]
	v_mfma_f32_16x16x128_f8f6f4 v[0:3], v[154:161], v[48:55], v[0:3]
	v_mfma_f32_16x16x128_f8f6f4 v[104:107], v[146:153], v[56:63], v[104:107]
	v_mfma_f32_16x16x128_f8f6f4 v[108:111], v[154:161], v[56:63], v[108:111]
	v_mfma_f32_16x16x128_f8f6f4 v[112:115], v[146:153], v[64:71], v[112:115]
	v_mfma_f32_16x16x128_f8f6f4 v[116:119], v[154:161], v[64:71], v[116:119]
	v_mfma_f32_16x16x128_f8f6f4 v[120:123], v[146:153], v[72:79], v[120:123]
	v_mfma_f32_16x16x128_f8f6f4 v[124:127], v[154:161], v[72:79], v[124:127]
	s_setprio 0
	s_barrier
	s_add_i32 s43, 0, 0x18000
	v_add_u32_e32 v48, s43, v194
	s_add_i32 s75, 0, 0x1c000
	v_add_u32_e32 v49, s43, v195
	ds_read_b128 v[130:133], v48
	ds_read_b128 v[138:141], v48 offset:2048
	ds_read_b128 v[134:137], v49
	ds_read_b128 v[142:145], v49 offset:2048
	v_add_u32_e32 v48, s75, v194
	v_add_u32_e32 v49, s75, v195
	ds_read_b128 v[146:149], v48
	ds_read_b128 v[154:157], v48 offset:2048
	ds_read_b128 v[150:153], v49
	ds_read_b128 v[158:161], v49 offset:2048
	s_mov_b32 m0, s52
	v_mov_b32_e32 v176, v129
	ds_read_b128 v[48:51], v227 offset:32768
	ds_read_b128 v[162:165], v227 offset:34816
	ds_read_b128 v[52:55], v228 offset:32768
	ds_read_b128 v[166:169], v228 offset:34816
	ds_read_b128 v[196:199], v227 offset:36864
	ds_read_b128 v[232:235], v227 offset:38912
	ds_read_b128 v[200:203], v228 offset:36864
	ds_read_b128 v[236:239], v228 offset:38912
	s_mov_b32 m0, s50
	s_nop 0
	global_load_lds_dwordx4 v180, s[38:39]
	s_mov_b32 m0, s51
	s_nop 0
	global_load_lds_dwordx4 v182, s[38:39]
	s_mov_b32 m0, s52
	v_mov_b32_e32 v186, v128
	global_load_lds_dwordx4 v176, s[38:39]
	s_mov_b32 m0, s53
	s_nop 0
	global_load_lds_dwordx4 v186, s[38:39]
	s_waitcnt vmcnt(8)
	s_waitcnt lgkmcnt(0)
	s_barrier
	s_setprio 1
	s_waitcnt lgkmcnt(0)
	v_mfma_f32_16x16x128_f8f6f4 v[100:103], v[130:137], v[48:55], v[100:103]
	v_mfma_f32_16x16x128_f8f6f4 v[96:99], v[138:145], v[48:55], v[96:99]
	v_mfma_f32_16x16x128_f8f6f4 v[92:95], v[130:137], v[162:169], v[92:95]
	v_mfma_f32_16x16x128_f8f6f4 v[88:91], v[138:145], v[162:169], v[88:91]
	v_mfma_f32_16x16x128_f8f6f4 v[84:87], v[130:137], v[196:203], v[84:87]
	v_mfma_f32_16x16x128_f8f6f4 v[80:83], v[138:145], v[196:203], v[80:83]
	v_mfma_f32_16x16x128_f8f6f4 v[76:79], v[130:137], v[232:239], v[170:173]
	v_mfma_f32_16x16x128_f8f6f4 v[72:75], v[138:145], v[232:239], v[188:191]
	s_setprio 0
	s_setprio 1
	v_mfma_f32_16x16x128_f8f6f4 v[68:71], v[146:153], v[48:55], v[248:251]
	v_mfma_f32_16x16x128_f8f6f4 v[64:67], v[154:161], v[48:55], v[204:207]
	v_mfma_f32_16x16x128_f8f6f4 v[60:63], v[146:153], v[162:169], v[208:211]
	v_mfma_f32_16x16x128_f8f6f4 v[56:59], v[154:161], v[162:169], v[212:215]
	v_mfma_f32_16x16x128_f8f6f4 v[52:55], v[146:153], v[196:203], v[216:219]
	v_mfma_f32_16x16x128_f8f6f4 v[48:51], v[154:161], v[196:203], v[240:243]
	v_mfma_f32_16x16x128_f8f6f4 v[40:43], v[146:153], v[232:239], v[40:43]
	v_mfma_f32_16x16x128_f8f6f4 v[32:35], v[154:161], v[232:239], v[32:35]
	s_setprio 0
	s_barrier
	v_mov_b32_e32 v185, v177
	ds_read_b128 v[162:165], v227 offset:49152
	ds_read_b128 v[196:199], v227 offset:51200
	ds_read_b128 v[166:169], v228 offset:49152
	ds_read_b128 v[200:203], v228 offset:51200
	ds_read_b128 v[232:235], v227 offset:53248
	ds_read_b128 v[240:243], v227 offset:55296
	ds_read_b128 v[236:239], v228 offset:53248
	ds_read_b128 v[244:247], v228 offset:55296
	s_add_i32 s43, s43, s5
	s_add_u32 vcc_lo, s40, s14
	s_addc_u32 vcc_hi, s41, s15
	s_mov_b32 m0, s43
	v_mov_b32_e32 v179, v177
	global_load_lds_dwordx4 v184, vcc
	s_add_i32 m0, s43, 0x2000
	v_mov_b32_e32 v181, v177
	global_load_lds_dwordx4 v178, vcc
	v_mov_b32_e32 v183, v177
	s_mov_b32 m0, s62
	s_add_u32 vcc_lo, s38, s14
	s_addc_u32 vcc_hi, s39, s15
	global_load_lds_dwordx4 v180, vcc
	s_mov_b32 m0, s63
	s_nop 0
	global_load_lds_dwordx4 v182, vcc
	s_waitcnt vmcnt(6)
	s_waitcnt lgkmcnt(0)
	s_barrier
	s_setprio 1
	s_waitcnt lgkmcnt(0)
	v_mfma_f32_16x16x128_f8f6f4 v[44:47], v[130:137], v[162:169], v[44:47]
	v_mfma_f32_16x16x128_f8f6f4 v[36:39], v[138:145], v[162:169], v[36:39]
	v_mfma_f32_16x16x128_f8f6f4 v[28:31], v[130:137], v[196:203], v[28:31]
	v_mfma_f32_16x16x128_f8f6f4 v[24:27], v[138:145], v[196:203], v[24:27]
	v_mfma_f32_16x16x128_f8f6f4 v[20:23], v[130:137], v[232:239], v[20:23]
	v_mfma_f32_16x16x128_f8f6f4 v[16:19], v[138:145], v[232:239], v[16:19]
	v_mfma_f32_16x16x128_f8f6f4 v[12:15], v[130:137], v[240:247], v[12:15]
	v_mfma_f32_16x16x128_f8f6f4 v[8:11], v[138:145], v[240:247], v[8:11]
	s_setprio 0
	s_setprio 1
	v_mfma_f32_16x16x128_f8f6f4 v[4:7], v[146:153], v[162:169], v[4:7]
	v_mfma_f32_16x16x128_f8f6f4 v[0:3], v[154:161], v[162:169], v[0:3]
	v_mfma_f32_16x16x128_f8f6f4 v[104:107], v[146:153], v[196:203], v[104:107]
	v_mfma_f32_16x16x128_f8f6f4 v[108:111], v[154:161], v[196:203], v[108:111]
	v_mfma_f32_16x16x128_f8f6f4 v[112:115], v[146:153], v[232:239], v[112:115]
	v_mfma_f32_16x16x128_f8f6f4 v[116:119], v[154:161], v[232:239], v[116:119]
	v_mfma_f32_16x16x128_f8f6f4 v[120:123], v[146:153], v[240:247], v[120:123]
	v_mfma_f32_16x16x128_f8f6f4 v[124:127], v[154:161], v[240:247], v[124:127]
	s_setprio 0
	s_barrier
	s_add_i32 s42, s42, 2
	s_add_u32 s36, s36, 0x100
	s_addc_u32 s37, s37, 0
	s_cmp_gt_u32 s42, 13
	s_cbranch_scc1 .LBB0_914

.LBB0_1008:
	s_add_u32 s5, s38, 0x100
	s_addc_u32 s27, s39, 0
	s_lshl_b32 s44, s61, 8
	s_lshl_b32 s29, s61, 19
	s_bitset1_b32 s44, 7
	s_mov_b32 s45, -2
	s_mov_b64 s[38:39], 0
	s_cmp_eq_u32 s45, 12
	s_cselect_b64 s[42:43], -1, 0
	s_and_b64 s[40:41], s[36:37], s[42:43]
	s_andn2_b64 vcc, exec, s[40:41]
	v_mov_b32_e32 v131, v138
	v_mov_b32_e32 v133, v128
	v_add_u32_e32 v135, s58, v142
	s_add_u32 s64, s6, s38
	v_add_u32_e32 v137, s58, v143
	ds_read_b128 v[178:181], v135
	ds_read_b128 v[186:189], v135 offset:2048
	ds_read_b128 v[182:185], v137
	ds_read_b128 v[190:193], v137 offset:2048
	v_add_u32_e32 v135, s59, v142
	s_addc_u32 s65, s7, s39
	v_add_u32_e32 v137, s59, v143
	ds_read_b128 v[194:197], v135
	ds_read_b128 v[202:205], v135 offset:2048
	ds_read_b128 v[198:201], v137
	ds_read_b128 v[206:209], v137 offset:2048
	s_add_u32 s66, s64, 0x5e000100
	s_addc_u32 s67, s65, 0
	s_and_b64 s[40:41], s[42:43], exec
	s_cselect_b32 s41, s11, s67
	s_cselect_b32 s40, s10, s66
	s_add_u32 s66, s5, s38
	s_addc_u32 s67, s27, s39
	s_and_b64 s[42:43], s[42:43], exec
	s_cselect_b32 s43, s35, s67
	s_cselect_b32 s42, s34, s66
	ds_read_b128 v[210:213], v175
	ds_read_b128 v[218:221], v175 offset:2048
	ds_read_b128 v[214:217], v176
	ds_read_b128 v[222:225], v176 offset:2048
	ds_read_b128 v[226:229], v175 offset:4096
	ds_read_b128 v[234:237], v175 offset:6144
	ds_read_b128 v[230:233], v176 offset:4096
	ds_read_b128 v[238:241], v176 offset:6144
	s_add_u32 vcc_lo, s66, 0x3f80
	s_addc_u32 vcc_hi, s67, 0
	s_add_i32 m0, s48, 0x1c000
	s_nop 0
	global_load_lds_dwordx4 v136, vcc
	s_add_i32 m0, s48, 0x1e000
	s_nop 0
	global_load_lds_dwordx4 v130, vcc
	s_add_i32 m0, s1, 0xc000
	s_add_u32 vcc_lo, s64, s16
	s_addc_u32 vcc_hi, s65, s17
	global_load_lds_dwordx4 v128, vcc
	v_mov_b32_e32 v139, v129
	s_add_i32 m0, s1, 0xe000
	s_nop 0
	global_load_lds_dwordx4 v138, vcc
	s_waitcnt vmcnt(8)
	s_waitcnt lgkmcnt(0)
	s_barrier
	s_setprio 1
	s_waitcnt lgkmcnt(0)
	v_mfma_f32_16x16x128_f8f6f4 v[100:103], v[178:185], v[210:217], 0
	v_mfma_f32_16x16x128_f8f6f4 v[96:99], v[186:193], v[210:217], 0
	v_mfma_f32_16x16x128_f8f6f4 v[92:95], v[178:185], v[218:225], 0
	v_mfma_f32_16x16x128_f8f6f4 v[88:91], v[186:193], v[218:225], 0
	v_mfma_f32_16x16x128_f8f6f4 v[84:87], v[178:185], v[226:233], 0
	v_mfma_f32_16x16x128_f8f6f4 v[80:83], v[186:193], v[226:233], 0
	v_mfma_f32_16x16x128_f8f6f4 v[242:245], v[178:185], v[234:241], 0
	v_mfma_f32_16x16x128_f8f6f4 v[246:249], v[186:193], v[234:241], 0
	s_setprio 0
	s_setprio 1
	v_mfma_f32_16x16x128_f8f6f4 v[40:43], v[194:201], v[234:241], 0
	v_mfma_f32_16x16x128_f8f6f4 v[32:35], v[202:209], v[234:241], 0
	v_mfma_f32_16x16x128_f8f6f4 v[250:253], v[194:201], v[210:217], 0
	v_mfma_f32_16x16x128_f8f6f4 v[144:147], v[202:209], v[210:217], 0
	v_mfma_f32_16x16x128_f8f6f4 v[148:151], v[194:201], v[218:225], 0
	v_mfma_f32_16x16x128_f8f6f4 v[152:155], v[202:209], v[218:225], 0
	v_mfma_f32_16x16x128_f8f6f4 v[156:159], v[194:201], v[226:233], 0
	v_mfma_f32_16x16x128_f8f6f4 v[160:163], v[202:209], v[226:233], 0
	s_setprio 0
	s_barrier
	s_add_i32 s64, s58, s48
	s_mov_b32 m0, s64
	s_nop 2
	ds_read_b128 v[48:51], v175 offset:16384
	ds_read_b128 v[56:59], v175 offset:18432
	ds_read_b128 v[52:55], v176 offset:16384
	ds_read_b128 v[60:63], v176 offset:18432
	ds_read_b128 v[64:67], v175 offset:20480
	ds_read_b128 v[72:75], v175 offset:22528
	ds_read_b128 v[68:71], v176 offset:20480
	ds_read_b128 v[76:79], v176 offset:22528
	s_nop 0
	global_load_lds_dwordx4 v136, s[42:43]
	s_add_i32 m0, s64, 0x2000
	s_add_u32 s64, s42, 0x4000
	s_addc_u32 s65, s43, 0
	s_add_i32 s66, s59, s48
	s_nop 0
	global_load_lds_dwordx4 v130, s[42:43]
	s_mov_b32 m0, s66
	s_nop 0
	global_load_lds_dwordx4 v136, s[64:65]
	s_add_i32 m0, s66, 0x2000
	s_nop 0
	global_load_lds_dwordx4 v130, s[64:65]
	s_waitcnt vmcnt(6)
	s_waitcnt lgkmcnt(0)
	s_barrier
	s_setprio 1
	s_waitcnt lgkmcnt(0)
	v_mfma_f32_16x16x128_f8f6f4 v[44:47], v[178:185], v[48:55], 0
	v_mfma_f32_16x16x128_f8f6f4 v[36:39], v[186:193], v[48:55], 0
	v_mfma_f32_16x16x128_f8f6f4 v[28:31], v[178:185], v[56:63], 0
	v_mfma_f32_16x16x128_f8f6f4 v[24:27], v[186:193], v[56:63], 0
	v_mfma_f32_16x16x128_f8f6f4 v[20:23], v[178:185], v[64:71], 0
	v_mfma_f32_16x16x128_f8f6f4 v[16:19], v[186:193], v[64:71], 0
	v_mfma_f32_16x16x128_f8f6f4 v[12:15], v[178:185], v[72:79], 0
	v_mfma_f32_16x16x128_f8f6f4 v[8:11], v[186:193], v[72:79], 0
	s_setprio 0
	s_setprio 1
	v_mfma_f32_16x16x128_f8f6f4 v[4:7], v[194:201], v[48:55], 0
	v_mfma_f32_16x16x128_f8f6f4 v[0:3], v[202:209], v[48:55], 0
	v_mfma_f32_16x16x128_f8f6f4 v[104:107], v[194:201], v[56:63], 0
	v_mfma_f32_16x16x128_f8f6f4 v[108:111], v[202:209], v[56:63], 0
	v_mfma_f32_16x16x128_f8f6f4 v[112:115], v[194:201], v[64:71], 0
	v_mfma_f32_16x16x128_f8f6f4 v[116:119], v[202:209], v[64:71], 0
	v_mfma_f32_16x16x128_f8f6f4 v[120:123], v[194:201], v[72:79], 0
	v_mfma_f32_16x16x128_f8f6f4 v[124:127], v[202:209], v[72:79], 0
	s_setprio 0
	s_barrier
	s_add_i32 s64, 0, 0x18000
	v_add_u32_e32 v48, s64, v142
	s_add_i32 s65, 0, 0x1c000
	v_add_u32_e32 v49, s64, v143
	ds_read_b128 v[178:181], v48
	ds_read_b128 v[186:189], v48 offset:2048
	ds_read_b128 v[182:185], v49
	ds_read_b128 v[190:193], v49 offset:2048
	v_add_u32_e32 v48, s65, v142
	v_add_u32_e32 v49, s65, v143
	ds_read_b128 v[194:197], v48
	ds_read_b128 v[202:205], v48 offset:2048
	ds_read_b128 v[198:201], v49
	ds_read_b128 v[206:209], v49 offset:2048
	s_mov_b32 m0, s50
	v_mov_b32_e32 v128, v133
	ds_read_b128 v[48:51], v175 offset:32768
	ds_read_b128 v[210:213], v175 offset:34816
	ds_read_b128 v[52:55], v176 offset:32768
	ds_read_b128 v[214:217], v176 offset:34816
	ds_read_b128 v[218:221], v175 offset:36864
	ds_read_b128 v[226:229], v175 offset:38912
	ds_read_b128 v[222:225], v176 offset:36864
	ds_read_b128 v[230:233], v176 offset:38912
	s_mov_b32 m0, s1
	s_nop 0
	global_load_lds_dwordx4 v132, s[40:41]
	s_mov_b32 m0, s49
	s_nop 0
	global_load_lds_dwordx4 v134, s[40:41]
	s_mov_b32 m0, s50
	v_mov_b32_e32 v138, v131
	global_load_lds_dwordx4 v128, s[40:41]
	s_mov_b32 m0, s51
	s_nop 0
	global_load_lds_dwordx4 v138, s[40:41]
	s_waitcnt vmcnt(8)
	s_waitcnt lgkmcnt(0)
	s_barrier
	s_setprio 1
	s_waitcnt lgkmcnt(0)
	v_mfma_f32_16x16x128_f8f6f4 v[100:103], v[178:185], v[48:55], v[100:103]
	v_mfma_f32_16x16x128_f8f6f4 v[96:99], v[186:193], v[48:55], v[96:99]
	v_mfma_f32_16x16x128_f8f6f4 v[92:95], v[178:185], v[210:217], v[92:95]
	v_mfma_f32_16x16x128_f8f6f4 v[88:91], v[186:193], v[210:217], v[88:91]
	v_mfma_f32_16x16x128_f8f6f4 v[84:87], v[178:185], v[218:225], v[84:87]
	v_mfma_f32_16x16x128_f8f6f4 v[80:83], v[186:193], v[218:225], v[80:83]
	v_mfma_f32_16x16x128_f8f6f4 v[76:79], v[178:185], v[226:233], v[242:245]
	v_mfma_f32_16x16x128_f8f6f4 v[72:75], v[186:193], v[226:233], v[246:249]
	s_setprio 0
	s_setprio 1
	v_mfma_f32_16x16x128_f8f6f4 v[68:71], v[194:201], v[48:55], v[250:253]
	v_mfma_f32_16x16x128_f8f6f4 v[64:67], v[202:209], v[48:55], v[144:147]
	v_mfma_f32_16x16x128_f8f6f4 v[60:63], v[194:201], v[210:217], v[148:151]
	v_mfma_f32_16x16x128_f8f6f4 v[56:59], v[202:209], v[210:217], v[152:155]
	v_mfma_f32_16x16x128_f8f6f4 v[52:55], v[194:201], v[218:225], v[156:159]
	v_mfma_f32_16x16x128_f8f6f4 v[48:51], v[202:209], v[218:225], v[160:163]
	v_mfma_f32_16x16x128_f8f6f4 v[40:43], v[194:201], v[226:233], v[40:43]
	v_mfma_f32_16x16x128_f8f6f4 v[32:35], v[202:209], v[226:233], v[32:35]
	s_setprio 0
	s_barrier
	v_mov_b32_e32 v137, v129
	ds_read_b128 v[210:213], v175 offset:49152
	ds_read_b128 v[218:221], v175 offset:51200
	ds_read_b128 v[214:217], v176 offset:49152
	ds_read_b128 v[222:225], v176 offset:51200
	ds_read_b128 v[226:229], v175 offset:53248
	ds_read_b128 v[234:237], v175 offset:55296
	ds_read_b128 v[230:233], v176 offset:53248
	ds_read_b128 v[238:241], v176 offset:55296
	s_add_i32 s64, s64, s48
	s_add_u32 vcc_lo, s42, s14
	s_addc_u32 vcc_hi, s43, s15
	s_mov_b32 m0, s64
	v_mov_b32_e32 v131, v129
	global_load_lds_dwordx4 v136, vcc
	s_add_i32 m0, s64, 0x2000
	v_mov_b32_e32 v133, v129
	global_load_lds_dwordx4 v130, vcc
	v_mov_b32_e32 v135, v129
	s_mov_b32 m0, s53
	s_add_u32 vcc_lo, s40, s14
	s_addc_u32 vcc_hi, s41, s15
	global_load_lds_dwordx4 v132, vcc
	s_mov_b32 m0, s54
	s_nop 0
	global_load_lds_dwordx4 v134, vcc
	s_waitcnt vmcnt(6)
	s_waitcnt lgkmcnt(0)
	s_barrier
	s_setprio 1
	s_waitcnt lgkmcnt(0)
	v_mfma_f32_16x16x128_f8f6f4 v[44:47], v[178:185], v[210:217], v[44:47]
	v_mfma_f32_16x16x128_f8f6f4 v[36:39], v[186:193], v[210:217], v[36:39]
	v_mfma_f32_16x16x128_f8f6f4 v[28:31], v[178:185], v[218:225], v[28:31]
	v_mfma_f32_16x16x128_f8f6f4 v[24:27], v[186:193], v[218:225], v[24:27]
	v_mfma_f32_16x16x128_f8f6f4 v[20:23], v[178:185], v[226:233], v[20:23]
	v_mfma_f32_16x16x128_f8f6f4 v[16:19], v[186:193], v[226:233], v[16:19]
	v_mfma_f32_16x16x128_f8f6f4 v[12:15], v[178:185], v[234:241], v[12:15]
	v_mfma_f32_16x16x128_f8f6f4 v[8:11], v[186:193], v[234:241], v[8:11]
	s_setprio 0
	s_setprio 1
	v_mfma_f32_16x16x128_f8f6f4 v[4:7], v[194:201], v[210:217], v[4:7]
	v_mfma_f32_16x16x128_f8f6f4 v[0:3], v[202:209], v[210:217], v[0:3]
	v_mfma_f32_16x16x128_f8f6f4 v[104:107], v[194:201], v[218:225], v[104:107]
	v_mfma_f32_16x16x128_f8f6f4 v[108:111], v[202:209], v[218:225], v[108:111]
	v_mfma_f32_16x16x128_f8f6f4 v[112:115], v[194:201], v[226:233], v[112:115]
	v_mfma_f32_16x16x128_f8f6f4 v[116:119], v[202:209], v[226:233], v[116:119]
	v_mfma_f32_16x16x128_f8f6f4 v[120:123], v[194:201], v[234:241], v[120:123]
	v_mfma_f32_16x16x128_f8f6f4 v[124:127], v[202:209], v[234:241], v[124:127]
	s_setprio 0
	s_barrier
	s_add_i32 s45, s45, 2
	s_add_u32 s38, s38, 0x100
	s_addc_u32 s39, s39, 0
	s_branch .LBB0_1010
.LBB0_1009:
	v_add_u32_e32 v135, s58, v142
	s_add_u32 s64, s6, s38
	v_add_u32_e32 v137, s58, v143
	ds_read_b128 v[178:181], v135
	ds_read_b128 v[186:189], v135 offset:2048
	ds_read_b128 v[182:185], v137
	ds_read_b128 v[190:193], v137 offset:2048
	v_add_u32_e32 v135, s59, v142
	s_addc_u32 s65, s7, s39
	v_add_u32_e32 v137, s59, v143
	ds_read_b128 v[194:197], v135
	ds_read_b128 v[202:205], v135 offset:2048
	ds_read_b128 v[198:201], v137
	ds_read_b128 v[206:209], v137 offset:2048
	s_add_u32 s66, s64, 0x5e000100
	s_addc_u32 s67, s65, 0
	s_and_b64 s[40:41], s[42:43], exec
	s_cselect_b32 s41, s11, s67
	s_cselect_b32 s40, s10, s66
	s_add_u32 s66, s5, s38
	s_addc_u32 s67, s27, s39
	s_and_b64 s[42:43], s[42:43], exec
	s_cselect_b32 s43, s35, s67
	s_cselect_b32 s42, s34, s66
	ds_read_b128 v[210:213], v175
	ds_read_b128 v[218:221], v175 offset:2048
	ds_read_b128 v[214:217], v176
	ds_read_b128 v[222:225], v176 offset:2048
	ds_read_b128 v[226:229], v175 offset:4096
	ds_read_b128 v[234:237], v175 offset:6144
	ds_read_b128 v[230:233], v176 offset:4096
	ds_read_b128 v[238:241], v176 offset:6144
	s_add_u32 vcc_lo, s66, 0x3f80
	s_addc_u32 vcc_hi, s67, 0
	s_add_i32 m0, s48, 0x1c000
	s_nop 0
	global_load_lds_dwordx4 v136, vcc
	s_add_i32 m0, s48, 0x1e000
	s_nop 0
	global_load_lds_dwordx4 v130, vcc
	s_add_i32 m0, s1, 0xc000
	s_add_u32 vcc_lo, s64, s16
	s_addc_u32 vcc_hi, s65, s17
	global_load_lds_dwordx4 v128, vcc
	v_mov_b32_e32 v139, v129
	s_add_i32 m0, s1, 0xe000
	s_nop 0
	global_load_lds_dwordx4 v138, vcc
	s_waitcnt vmcnt(8)
	s_waitcnt lgkmcnt(0)
	s_barrier
	s_setprio 1
	s_waitcnt lgkmcnt(0)
	v_mfma_f32_16x16x128_f8f6f4 v[100:103], v[178:185], v[210:217], v[100:103]
	v_mfma_f32_16x16x128_f8f6f4 v[96:99], v[186:193], v[210:217], v[96:99]
	v_mfma_f32_16x16x128_f8f6f4 v[92:95], v[178:185], v[218:225], v[92:95]
	v_mfma_f32_16x16x128_f8f6f4 v[88:91], v[186:193], v[218:225], v[88:91]
	v_mfma_f32_16x16x128_f8f6f4 v[84:87], v[178:185], v[226:233], v[84:87]
	v_mfma_f32_16x16x128_f8f6f4 v[80:83], v[186:193], v[226:233], v[80:83]
	v_mfma_f32_16x16x128_f8f6f4 v[242:245], v[178:185], v[234:241], v[76:79]
	v_mfma_f32_16x16x128_f8f6f4 v[246:249], v[186:193], v[234:241], v[72:75]
	s_setprio 0
	s_setprio 1
	v_mfma_f32_16x16x128_f8f6f4 v[40:43], v[194:201], v[234:241], v[40:43]
	v_mfma_f32_16x16x128_f8f6f4 v[32:35], v[202:209], v[234:241], v[32:35]
	v_mfma_f32_16x16x128_f8f6f4 v[250:253], v[194:201], v[210:217], v[68:71]
	v_mfma_f32_16x16x128_f8f6f4 v[144:147], v[202:209], v[210:217], v[64:67]
	v_mfma_f32_16x16x128_f8f6f4 v[148:151], v[194:201], v[218:225], v[60:63]
	v_mfma_f32_16x16x128_f8f6f4 v[152:155], v[202:209], v[218:225], v[56:59]
	v_mfma_f32_16x16x128_f8f6f4 v[156:159], v[194:201], v[226:233], v[52:55]
	v_mfma_f32_16x16x128_f8f6f4 v[160:163], v[202:209], v[226:233], v[48:51]
	s_setprio 0
	s_barrier
	s_add_i32 s64, s58, s48
	s_mov_b32 m0, s64
	s_nop 2
	ds_read_b128 v[48:51], v175 offset:16384
	ds_read_b128 v[56:59], v175 offset:18432
	ds_read_b128 v[52:55], v176 offset:16384
	ds_read_b128 v[60:63], v176 offset:18432
	ds_read_b128 v[64:67], v175 offset:20480
	ds_read_b128 v[72:75], v175 offset:22528
	ds_read_b128 v[68:71], v176 offset:20480
	ds_read_b128 v[76:79], v176 offset:22528
	s_nop 0
	global_load_lds_dwordx4 v136, s[42:43]
	s_add_i32 m0, s64, 0x2000
	s_add_u32 s64, s42, 0x4000
	s_addc_u32 s65, s43, 0
	s_add_i32 s66, s59, s48
	s_nop 0
	global_load_lds_dwordx4 v130, s[42:43]
	s_mov_b32 m0, s66
	s_nop 0
	global_load_lds_dwordx4 v136, s[64:65]
	s_add_i32 m0, s66, 0x2000
	s_nop 0
	global_load_lds_dwordx4 v130, s[64:65]
	s_waitcnt vmcnt(6)
	s_waitcnt lgkmcnt(0)
	s_barrier
	s_setprio 1
	s_waitcnt lgkmcnt(0)
	v_mfma_f32_16x16x128_f8f6f4 v[44:47], v[178:185], v[48:55], v[44:47]
	v_mfma_f32_16x16x128_f8f6f4 v[36:39], v[186:193], v[48:55], v[36:39]
	v_mfma_f32_16x16x128_f8f6f4 v[28:31], v[178:185], v[56:63], v[28:31]
	v_mfma_f32_16x16x128_f8f6f4 v[24:27], v[186:193], v[56:63], v[24:27]
	v_mfma_f32_16x16x128_f8f6f4 v[20:23], v[178:185], v[64:71], v[20:23]
	v_mfma_f32_16x16x128_f8f6f4 v[16:19], v[186:193], v[64:71], v[16:19]
	v_mfma_f32_16x16x128_f8f6f4 v[12:15], v[178:185], v[72:79], v[12:15]
	v_mfma_f32_16x16x128_f8f6f4 v[8:11], v[186:193], v[72:79], v[8:11]
	s_setprio 0
	s_setprio 1
	v_mfma_f32_16x16x128_f8f6f4 v[4:7], v[194:201], v[48:55], v[4:7]
	v_mfma_f32_16x16x128_f8f6f4 v[0:3], v[202:209], v[48:55], v[0:3]
	v_mfma_f32_16x16x128_f8f6f4 v[104:107], v[194:201], v[56:63], v[104:107]
	v_mfma_f32_16x16x128_f8f6f4 v[108:111], v[202:209], v[56:63], v[108:111]
	v_mfma_f32_16x16x128_f8f6f4 v[112:115], v[194:201], v[64:71], v[112:115]
	v_mfma_f32_16x16x128_f8f6f4 v[116:119], v[202:209], v[64:71], v[116:119]
	v_mfma_f32_16x16x128_f8f6f4 v[120:123], v[194:201], v[72:79], v[120:123]
	v_mfma_f32_16x16x128_f8f6f4 v[124:127], v[202:209], v[72:79], v[124:127]
	s_setprio 0
	s_barrier
	s_add_i32 s64, 0, 0x18000
	v_add_u32_e32 v48, s64, v142
	s_add_i32 s65, 0, 0x1c000
	v_add_u32_e32 v49, s64, v143
	ds_read_b128 v[178:181], v48
	ds_read_b128 v[186:189], v48 offset:2048
	ds_read_b128 v[182:185], v49
	ds_read_b128 v[190:193], v49 offset:2048
	v_add_u32_e32 v48, s65, v142
	v_add_u32_e32 v49, s65, v143
	ds_read_b128 v[194:197], v48
	ds_read_b128 v[202:205], v48 offset:2048
	ds_read_b128 v[198:201], v49
	ds_read_b128 v[206:209], v49 offset:2048
	s_mov_b32 m0, s50
	v_mov_b32_e32 v128, v133
	ds_read_b128 v[48:51], v175 offset:32768
	ds_read_b128 v[210:213], v175 offset:34816
	ds_read_b128 v[52:55], v176 offset:32768
	ds_read_b128 v[214:217], v176 offset:34816
	ds_read_b128 v[218:221], v175 offset:36864
	ds_read_b128 v[226:229], v175 offset:38912
	ds_read_b128 v[222:225], v176 offset:36864
	ds_read_b128 v[230:233], v176 offset:38912
	s_mov_b32 m0, s1
	s_nop 0
	global_load_lds_dwordx4 v132, s[40:41]
	s_mov_b32 m0, s49
	s_nop 0
	global_load_lds_dwordx4 v134, s[40:41]
	s_mov_b32 m0, s50
	v_mov_b32_e32 v138, v131
	global_load_lds_dwordx4 v128, s[40:41]
	s_mov_b32 m0, s51
	s_nop 0
	global_load_lds_dwordx4 v138, s[40:41]
	s_waitcnt vmcnt(8)
	s_waitcnt lgkmcnt(0)
	s_barrier
	s_setprio 1
	s_waitcnt lgkmcnt(0)
	v_mfma_f32_16x16x128_f8f6f4 v[100:103], v[178:185], v[48:55], v[100:103]
	v_mfma_f32_16x16x128_f8f6f4 v[96:99], v[186:193], v[48:55], v[96:99]
	v_mfma_f32_16x16x128_f8f6f4 v[92:95], v[178:185], v[210:217], v[92:95]
	v_mfma_f32_16x16x128_f8f6f4 v[88:91], v[186:193], v[210:217], v[88:91]
	v_mfma_f32_16x16x128_f8f6f4 v[84:87], v[178:185], v[218:225], v[84:87]
	v_mfma_f32_16x16x128_f8f6f4 v[80:83], v[186:193], v[218:225], v[80:83]
	v_mfma_f32_16x16x128_f8f6f4 v[76:79], v[178:185], v[226:233], v[242:245]
	v_mfma_f32_16x16x128_f8f6f4 v[72:75], v[186:193], v[226:233], v[246:249]
	s_setprio 0
	s_setprio 1
	v_mfma_f32_16x16x128_f8f6f4 v[68:71], v[194:201], v[48:55], v[250:253]
	v_mfma_f32_16x16x128_f8f6f4 v[64:67], v[202:209], v[48:55], v[144:147]
	v_mfma_f32_16x16x128_f8f6f4 v[60:63], v[194:201], v[210:217], v[148:151]
	v_mfma_f32_16x16x128_f8f6f4 v[56:59], v[202:209], v[210:217], v[152:155]
	v_mfma_f32_16x16x128_f8f6f4 v[52:55], v[194:201], v[218:225], v[156:159]
	v_mfma_f32_16x16x128_f8f6f4 v[48:51], v[202:209], v[218:225], v[160:163]
	v_mfma_f32_16x16x128_f8f6f4 v[40:43], v[194:201], v[226:233], v[40:43]
	v_mfma_f32_16x16x128_f8f6f4 v[32:35], v[202:209], v[226:233], v[32:35]
	s_setprio 0
	s_barrier
	v_mov_b32_e32 v137, v129
	ds_read_b128 v[210:213], v175 offset:49152
	ds_read_b128 v[218:221], v175 offset:51200
	ds_read_b128 v[214:217], v176 offset:49152
	ds_read_b128 v[222:225], v176 offset:51200
	ds_read_b128 v[226:229], v175 offset:53248
	ds_read_b128 v[234:237], v175 offset:55296
	ds_read_b128 v[230:233], v176 offset:53248
	ds_read_b128 v[238:241], v176 offset:55296
	s_add_i32 s64, s64, s48
	s_add_u32 vcc_lo, s42, s14
	s_addc_u32 vcc_hi, s43, s15
	s_mov_b32 m0, s64
	v_mov_b32_e32 v131, v129
	global_load_lds_dwordx4 v136, vcc
	s_add_i32 m0, s64, 0x2000
	v_mov_b32_e32 v133, v129
	global_load_lds_dwordx4 v130, vcc
	v_mov_b32_e32 v135, v129
	s_mov_b32 m0, s53
	s_add_u32 vcc_lo, s40, s14
	s_addc_u32 vcc_hi, s41, s15
	global_load_lds_dwordx4 v132, vcc
	s_mov_b32 m0, s54
	s_nop 0
	global_load_lds_dwordx4 v134, vcc
	s_waitcnt vmcnt(6)
	s_waitcnt lgkmcnt(0)
	s_barrier
	s_setprio 1
	s_waitcnt lgkmcnt(0)
	v_mfma_f32_16x16x128_f8f6f4 v[44:47], v[178:185], v[210:217], v[44:47]
	v_mfma_f32_16x16x128_f8f6f4 v[36:39], v[186:193], v[210:217], v[36:39]
	v_mfma_f32_16x16x128_f8f6f4 v[28:31], v[178:185], v[218:225], v[28:31]
	v_mfma_f32_16x16x128_f8f6f4 v[24:27], v[186:193], v[218:225], v[24:27]
	v_mfma_f32_16x16x128_f8f6f4 v[20:23], v[178:185], v[226:233], v[20:23]
	v_mfma_f32_16x16x128_f8f6f4 v[16:19], v[186:193], v[226:233], v[16:19]
	v_mfma_f32_16x16x128_f8f6f4 v[12:15], v[178:185], v[234:241], v[12:15]
	v_mfma_f32_16x16x128_f8f6f4 v[8:11], v[186:193], v[234:241], v[8:11]
	s_setprio 0
	s_setprio 1
	v_mfma_f32_16x16x128_f8f6f4 v[4:7], v[194:201], v[210:217], v[4:7]
	v_mfma_f32_16x16x128_f8f6f4 v[0:3], v[202:209], v[210:217], v[0:3]
	v_mfma_f32_16x16x128_f8f6f4 v[104:107], v[194:201], v[218:225], v[104:107]
	v_mfma_f32_16x16x128_f8f6f4 v[108:111], v[202:209], v[218:225], v[108:111]
	v_mfma_f32_16x16x128_f8f6f4 v[112:115], v[194:201], v[226:233], v[112:115]
	v_mfma_f32_16x16x128_f8f6f4 v[116:119], v[202:209], v[226:233], v[116:119]
	v_mfma_f32_16x16x128_f8f6f4 v[120:123], v[194:201], v[234:241], v[120:123]
	v_mfma_f32_16x16x128_f8f6f4 v[124:127], v[202:209], v[234:241], v[124:127]
	s_setprio 0
	s_barrier
	s_add_i32 s45, s45, 2
	s_add_u32 s38, s38, 0x100
	s_addc_u32 s39, s39, 0
	s_cmp_gt_u32 s45, 13
	s_cbranch_scc1 .LBB0_1012
